# P1 idle workgroups (two GEMM units) now convert 3 next-layer weight tiles instead of 2 (work-stealing quota), on top of barrier rewrite with L1-only acquire, LN1 preload, router prefetch
# speedup vs baseline: 1.0296x; 1.0055x over previous
; #define LAS __attribute__((address_space(3)))
; #define F8_LOADS() do { _Pragma("unroll") for (int q = 0; q < 32; ++q) v[q] = __builtin_nontemporal_load((const f32x4*)(T.src + (size_t)q * T.ld)); } while (0)
; template <bool STEAL>
; __device__ __forceinline__ void f8_convert(const Args& a, LAS unsigned char* lds, unsigned char* ws, int l, int first, int stride, int quota, unsigned* ticket, int tid, int lane, int wave) {
;     ...
;     if constexpr (STEAL) {
;         __syncthreads();
;         if (first != -2) {
;             if (tid == 0) word[0] = (quota > 0) ? (int)__hip_atomic_fetch_add(ticket, 1u, __ATOMIC_RELAXED, __HIP_MEMORY_SCOPE_AGENT) : F8_TILES_PER_LAYER;
;             __syncthreads(); }
;         k = word[0];
;     } else k = first;
;     F8Tile T = f8_tile(a, lds, ws, f8_tile_of(l, k < F8_TILES_PER_LAYER ? k : 0), lane, wave);
;     ...
;     if (k < F8_TILES_PER_LAYER) F8_LOADS();
;     while (k < F8_TILES_PER_LAYER) {
;         LAS unsigned char* buf = lds + (n & 1) * 65536;
;         if constexpr (STEAL) { if (tid == 0) word[(n + 1) & 1] = (n + 1 < quota) ? (int)__hip_atomic_fetch_add(ticket, 1u, __ATOMIC_RELAXED, __HIP_MEMORY_SCOPE_AGENT) : F8_TILES_PER_LAYER; }
.LBB0_247:
	s_and_saveexec_b64 s[2:3], s[0:1]
	s_xor_b64 s[2:3], exec, s[2:3]
	s_and_b32 s4, s35, 1
	s_or_saveexec_b64 s[2:3], s[2:3]
	v_mov_b32_e32 v152, s4
	s_xor_b64 exec, exec, s[2:3]
	s_cbranch_execz .LBB0_253
	s_cmp_gt_u32 s35, 2
	v_mov_b32_e32 v152, 0x6e0
	s_cbranch_scc1 .LBB0_252
	v_mov_b64_e32 v[152:153], s[6:7]
	flat_atomic_add v152, v[152:153], v206 sc0
